# grid barrier: last XCD leader bumps all per-XCD release words itself (one polling stage less); leaders no longer bump their own XCD word
# baseline (speedup 1.0000x reference)
.LBB0_188:
	s_or_b64 exec, exec, s[8:9]
	v_cvt_f32_u32_e32 v3, v0
	s_waitcnt vmcnt(0)
	v_readfirstlane_b32 s4, v2
	s_add_u32 s8, s46, 0x7500
	s_addc_u32 s9, s47, 0
	v_rcp_iflag_f32_e32 v3, v3
	v_add_u32_e32 v1, s4, v1
	v_add_u32_e32 v4, 1, v1
	s_mov_b64 s[10:11], -1
	v_mul_f32_e32 v2, 0x4f7ffffe, v3
	v_cvt_u32_f32_e32 v2, v2
	v_sub_u32_e32 v3, 0, v0
	v_mul_lo_u32 v3, v3, v2
	v_mul_hi_u32 v3, v2, v3
	v_add_u32_e32 v2, v2, v3
	v_mul_hi_u32 v2, v1, v2
	v_mul_lo_u32 v3, v2, v0
	v_sub_u32_e32 v1, v1, v3
	v_add_u32_e32 v5, 1, v2
	v_cmp_ge_u32_e32 vcc, v1, v0
	v_sub_u32_e32 v3, v1, v0
	s_nop 0
	v_cndmask_b32_e32 v2, v2, v5, vcc
	v_cndmask_b32_e32 v1, v1, v3, vcc
	v_add_u32_e32 v3, 1, v2
	v_cmp_ge_u32_e32 vcc, v1, v0
	s_nop 1
	v_cndmask_b32_e32 v2, v2, v3, vcc
	v_mul_lo_u32 v1, v0, v2
	v_add_u32_e32 v0, v1, v0
	v_cmp_ne_u32_e32 vcc, v4, v0
	s_cbranch_vccnz .Lxr_0
	v_readlane_b32 s98, v254, 9
	v_readlane_b32 s99, v254, 10
	v_mov_b32_e32 v100, 0x2400
	v_mov_b32_e32 v101, 1
	s_nop 4
	global_atomic_add v100, v101, s[98:99]
	global_atomic_add v100, v101, s[98:99] offset:256
	global_atomic_add v100, v101, s[98:99] offset:512
	global_atomic_add v100, v101, s[98:99] offset:768
	global_atomic_add v100, v101, s[98:99] offset:1024
	global_atomic_add v100, v101, s[98:99] offset:1280
	global_atomic_add v100, v101, s[98:99] offset:1536
	global_atomic_add v100, v101, s[98:99] offset:1792
	global_atomic_add v100, v101, s[98:99] offset:2048
	global_atomic_add v100, v101, s[98:99] offset:2304
	global_atomic_add v100, v101, s[98:99] offset:2560
	global_atomic_add v100, v101, s[98:99] offset:2816
	global_atomic_add v100, v101, s[98:99] offset:3072
	global_atomic_add v100, v101, s[98:99] offset:3328
	global_atomic_add v100, v101, s[98:99] offset:3584
	global_atomic_add v100, v101, s[98:99] offset:3840
.Lxr_0:
	v_mov_b64_e32 v[0:1], s[8:9]
	s_and_saveexec_b64 s[6:7], vcc
	s_cbranch_execz .LBB0_200
	v_mov_b32_e32 v0, 0
	global_load_dword v1, v0, s[8:9] sc1
	s_mov_b64 s[14:15], 0
	s_waitcnt vmcnt(0)
	v_cmp_eq_u32_e32 vcc, v1, v2
	s_and_saveexec_b64 s[12:13], vcc
	s_cbranch_execz .LBB0_199
	s_add_u32 s10, s46, 0x4200
	s_addc_u32 s11, s47, 0
	s_mov_b32 s22, 1
	s_mov_b64 s[4:5], 0
	s_branch .LBB0_192

.LBB0_202:
	s_or_b64 exec, exec, s[4:5]
	s_mov_b64 s[4:5], exec
	v_mbcnt_lo_u32_b32 v0, s4, 0
	v_mbcnt_hi_u32_b32 v0, s5, v0
	v_cmp_eq_u32_e32 vcc, 0, v0
	s_waitcnt vmcnt(0)
	s_and_saveexec_b64 s[6:7], vcc
	s_cbranch_execz .LBB0_204
	s_bcnt1_i32_b64 s4, s[4:5]
	v_mov_b32_e32 v0, 0x2000
	v_mov_b32_e32 v1, s4
.LBB0_204:
	s_or_b64 exec, exec, s[6:7]
	s_waitcnt vmcnt(0)

.LBB0_306:
	s_or_b64 exec, exec, s[6:7]
	s_waitcnt vmcnt(0)
	v_readfirstlane_b32 s4, v3
	v_sub_u32_e32 v4, 0, v2
	s_mov_b64 s[14:15], -1
	v_add_u32_e32 v3, s4, v0
	v_cvt_f32_u32_e32 v0, v2
	v_readlane_b32 s4, v254, 46
	v_readlane_b32 s5, v254, 47
	s_add_u32 s4, s4, 0x3500
	v_rcp_iflag_f32_e32 v0, v0
	s_addc_u32 s5, s5, 0
	v_mul_f32_e32 v0, 0x4f7ffffe, v0
	v_cvt_u32_f32_e32 v0, v0
	v_mul_lo_u32 v4, v4, v0
	v_mul_hi_u32 v4, v0, v4
	v_add_u32_e32 v0, v0, v4
	v_mul_hi_u32 v0, v3, v0
	v_mul_lo_u32 v4, v0, v2
	v_sub_u32_e32 v4, v3, v4
	v_cmp_ge_u32_e32 vcc, v4, v2
	v_add_u32_e32 v5, 1, v0
	v_add_u32_e32 v3, 1, v3
	v_cndmask_b32_e32 v0, v0, v5, vcc
	v_sub_u32_e32 v5, v4, v2
	v_cndmask_b32_e32 v4, v4, v5, vcc
	v_cmp_ge_u32_e32 vcc, v4, v2
	v_add_u32_e32 v4, 1, v0
	s_nop 0
	v_cndmask_b32_e32 v0, v0, v4, vcc
	v_mul_lo_u32 v4, v2, v0
	v_add_u32_e32 v2, v4, v2
	v_cmp_ne_u32_e32 vcc, v3, v2
	s_cbranch_vccnz .Lxr_1
	v_readlane_b32 s98, v254, 9
	v_readlane_b32 s99, v254, 10
	v_mov_b32_e32 v100, 0x2400
	v_mov_b32_e32 v101, 1
	s_nop 4
	global_atomic_add v100, v101, s[98:99]
	global_atomic_add v100, v101, s[98:99] offset:256
	global_atomic_add v100, v101, s[98:99] offset:512
	global_atomic_add v100, v101, s[98:99] offset:768
	global_atomic_add v100, v101, s[98:99] offset:1024
	global_atomic_add v100, v101, s[98:99] offset:1280
	global_atomic_add v100, v101, s[98:99] offset:1536
	global_atomic_add v100, v101, s[98:99] offset:1792
	global_atomic_add v100, v101, s[98:99] offset:2048
	global_atomic_add v100, v101, s[98:99] offset:2304
	global_atomic_add v100, v101, s[98:99] offset:2560
	global_atomic_add v100, v101, s[98:99] offset:2816
	global_atomic_add v100, v101, s[98:99] offset:3072
	global_atomic_add v100, v101, s[98:99] offset:3328
	global_atomic_add v100, v101, s[98:99] offset:3584
	global_atomic_add v100, v101, s[98:99] offset:3840
.Lxr_1:
	v_mov_b64_e32 v[2:3], s[4:5]
	s_and_saveexec_b64 s[6:7], vcc
	s_cbranch_execz .LBB0_318
	global_load_dword v2, v1, s[4:5] sc1
	s_mov_b64 s[16:17], 0
	s_waitcnt vmcnt(0)
	v_cmp_eq_u32_e32 vcc, v2, v0
	s_and_saveexec_b64 s[14:15], vcc
	s_cbranch_execz .LBB0_317
	v_readlane_b32 s10, v254, 46
	v_readlane_b32 s11, v254, 47
	s_add_u32 s16, s10, 0x200
	s_addc_u32 s17, s11, 0
	s_mov_b32 s10, 1
	s_mov_b64 s[22:23], 0
	s_branch .LBB0_310

.LBB0_320:
	s_or_b64 exec, exec, s[4:5]
	s_mov_b64 s[4:5], exec
	v_mbcnt_lo_u32_b32 v0, s4, 0
	v_mbcnt_hi_u32_b32 v0, s5, v0
	v_cmp_eq_u32_e32 vcc, 0, v0
	s_waitcnt vmcnt(0)
	s_and_saveexec_b64 s[6:7], vcc
	s_cbranch_execz .LBB0_322
	s_add_i32 s76, s9, 0x900
	s_lshl_b64 s[10:11], s[76:77], 2
	v_readlane_b32 s12, v254, 46
	v_readlane_b32 s13, v254, 47
	s_add_u32 s10, s12, s10
	s_addc_u32 s11, s13, s11
	s_bcnt1_i32_b64 s4, s[4:5]
	v_mov_b32_e32 v0, s4
.LBB0_322:
	s_or_b64 exec, exec, s[6:7]
	s_waitcnt vmcnt(0)

.LBB0_645:
	s_or_b64 exec, exec, s[6:7]
	s_waitcnt vmcnt(0)
	v_readfirstlane_b32 s2, v3
	v_sub_u32_e32 v4, 0, v2
	s_mov_b64 s[14:15], -1
	v_add_u32_e32 v3, s2, v0
	v_cvt_f32_u32_e32 v0, v2
	v_readlane_b32 s2, v254, 46
	v_readlane_b32 s3, v254, 47
	s_add_u32 s2, s2, 0x3500
	v_rcp_iflag_f32_e32 v0, v0
	s_addc_u32 s3, s3, 0
	v_mul_f32_e32 v0, 0x4f7ffffe, v0
	v_cvt_u32_f32_e32 v0, v0
	v_mul_lo_u32 v4, v4, v0
	v_mul_hi_u32 v4, v0, v4
	v_add_u32_e32 v0, v0, v4
	v_mul_hi_u32 v0, v3, v0
	v_mul_lo_u32 v4, v0, v2
	v_sub_u32_e32 v4, v3, v4
	v_cmp_ge_u32_e32 vcc, v4, v2
	v_add_u32_e32 v5, 1, v0
	v_add_u32_e32 v3, 1, v3
	v_cndmask_b32_e32 v0, v0, v5, vcc
	v_sub_u32_e32 v5, v4, v2
	v_cndmask_b32_e32 v4, v4, v5, vcc
	v_cmp_ge_u32_e32 vcc, v4, v2
	v_add_u32_e32 v4, 1, v0
	s_nop 0
	v_cndmask_b32_e32 v0, v0, v4, vcc
	v_mul_lo_u32 v4, v2, v0
	v_add_u32_e32 v2, v4, v2
	v_cmp_ne_u32_e32 vcc, v3, v2
	s_cbranch_vccnz .Lxr_2
	v_readlane_b32 s98, v254, 9
	v_readlane_b32 s99, v254, 10
	v_mov_b32_e32 v100, 0x2400
	v_mov_b32_e32 v101, 1
	s_nop 4
	global_atomic_add v100, v101, s[98:99]
	global_atomic_add v100, v101, s[98:99] offset:256
	global_atomic_add v100, v101, s[98:99] offset:512
	global_atomic_add v100, v101, s[98:99] offset:768
	global_atomic_add v100, v101, s[98:99] offset:1024
	global_atomic_add v100, v101, s[98:99] offset:1280
	global_atomic_add v100, v101, s[98:99] offset:1536
	global_atomic_add v100, v101, s[98:99] offset:1792
	global_atomic_add v100, v101, s[98:99] offset:2048
	global_atomic_add v100, v101, s[98:99] offset:2304
	global_atomic_add v100, v101, s[98:99] offset:2560
	global_atomic_add v100, v101, s[98:99] offset:2816
	global_atomic_add v100, v101, s[98:99] offset:3072
	global_atomic_add v100, v101, s[98:99] offset:3328
	global_atomic_add v100, v101, s[98:99] offset:3584
	global_atomic_add v100, v101, s[98:99] offset:3840
.Lxr_2:
	v_mov_b64_e32 v[2:3], s[2:3]
	s_and_saveexec_b64 s[6:7], vcc
	s_cbranch_execz .LBB0_657
	global_load_dword v2, v1, s[2:3] sc1
	s_mov_b64 s[16:17], 0
	s_waitcnt vmcnt(0)
	v_cmp_eq_u32_e32 vcc, v2, v0
	s_and_saveexec_b64 s[14:15], vcc
	s_cbranch_execz .LBB0_656
	v_readlane_b32 s10, v254, 46
	v_readlane_b32 s11, v254, 47
	s_add_u32 s16, s10, 0x200
	s_addc_u32 s17, s11, 0
	s_mov_b32 s9, 1
	s_mov_b64 s[18:19], 0
	s_branch .LBB0_649

.LBB0_659:
	s_or_b64 exec, exec, s[2:3]
	s_mov_b64 s[2:3], exec
	v_mbcnt_lo_u32_b32 v0, s2, 0
	v_mbcnt_hi_u32_b32 v0, s3, v0
	v_cmp_eq_u32_e32 vcc, 0, v0
	s_waitcnt vmcnt(0)
	s_and_saveexec_b64 s[6:7], vcc
	s_cbranch_execz .LBB0_661
	s_add_i32 s76, s8, 0x900
	s_lshl_b64 s[8:9], s[76:77], 2
	v_readlane_b32 s10, v254, 46
	v_readlane_b32 s11, v254, 47
	s_add_u32 s8, s10, s8
	s_addc_u32 s9, s11, s9
	s_bcnt1_i32_b64 s2, s[2:3]
	v_mov_b32_e32 v0, s2
.LBB0_661:
	s_or_b64 exec, exec, s[6:7]
	s_waitcnt vmcnt(0)

.LBB0_811:
	s_or_b64 exec, exec, s[10:11]
	s_waitcnt vmcnt(0)
	v_readfirstlane_b32 s6, v3
	v_sub_u32_e32 v4, 0, v2
	s_mov_b64 s[12:13], -1
	v_add_u32_e32 v3, s6, v0
	v_cvt_f32_u32_e32 v0, v2
	v_readlane_b32 s6, v254, 46
	v_readlane_b32 s7, v254, 47
	s_add_u32 s6, s6, 0x3500
	v_rcp_iflag_f32_e32 v0, v0
	s_addc_u32 s7, s7, 0
	v_mul_f32_e32 v0, 0x4f7ffffe, v0
	v_cvt_u32_f32_e32 v0, v0
	v_mul_lo_u32 v4, v4, v0
	v_mul_hi_u32 v4, v0, v4
	v_add_u32_e32 v0, v0, v4
	v_mul_hi_u32 v0, v3, v0
	v_mul_lo_u32 v4, v0, v2
	v_sub_u32_e32 v4, v3, v4
	v_cmp_ge_u32_e32 vcc, v4, v2
	v_add_u32_e32 v5, 1, v0
	v_add_u32_e32 v3, 1, v3
	v_cndmask_b32_e32 v0, v0, v5, vcc
	v_sub_u32_e32 v5, v4, v2
	v_cndmask_b32_e32 v4, v4, v5, vcc
	v_cmp_ge_u32_e32 vcc, v4, v2
	v_add_u32_e32 v4, 1, v0
	s_nop 0
	v_cndmask_b32_e32 v0, v0, v4, vcc
	v_mul_lo_u32 v4, v2, v0
	v_add_u32_e32 v2, v4, v2
	v_cmp_ne_u32_e32 vcc, v3, v2
	s_cbranch_vccnz .Lxr_3
	v_readlane_b32 s98, v254, 9
	v_readlane_b32 s99, v254, 10
	v_mov_b32_e32 v100, 0x2400
	v_mov_b32_e32 v101, 1
	s_nop 4
	global_atomic_add v100, v101, s[98:99]
	global_atomic_add v100, v101, s[98:99] offset:256
	global_atomic_add v100, v101, s[98:99] offset:512
	global_atomic_add v100, v101, s[98:99] offset:768
	global_atomic_add v100, v101, s[98:99] offset:1024
	global_atomic_add v100, v101, s[98:99] offset:1280
	global_atomic_add v100, v101, s[98:99] offset:1536
	global_atomic_add v100, v101, s[98:99] offset:1792
	global_atomic_add v100, v101, s[98:99] offset:2048
	global_atomic_add v100, v101, s[98:99] offset:2304
	global_atomic_add v100, v101, s[98:99] offset:2560
	global_atomic_add v100, v101, s[98:99] offset:2816
	global_atomic_add v100, v101, s[98:99] offset:3072
	global_atomic_add v100, v101, s[98:99] offset:3328
	global_atomic_add v100, v101, s[98:99] offset:3584
	global_atomic_add v100, v101, s[98:99] offset:3840
.Lxr_3:
	v_mov_b64_e32 v[2:3], s[6:7]
	s_and_saveexec_b64 s[10:11], vcc
	s_cbranch_execz .LBB0_823
	global_load_dword v2, v1, s[6:7] sc1
	s_mov_b64 s[14:15], 0
	s_waitcnt vmcnt(0)
	v_cmp_eq_u32_e32 vcc, v2, v0
	s_and_saveexec_b64 s[12:13], vcc
	s_cbranch_execz .LBB0_822
	v_readlane_b32 s14, v254, 46
	v_readlane_b32 s15, v254, 47
	s_add_u32 s14, s14, 0x200
	s_addc_u32 s15, s15, 0
	s_mov_b32 s9, 1
	s_mov_b64 s[16:17], 0
	s_branch .LBB0_815

.LBB0_825:
	s_or_b64 exec, exec, s[6:7]
	s_mov_b64 s[6:7], exec
	v_mbcnt_lo_u32_b32 v0, s6, 0
	v_mbcnt_hi_u32_b32 v0, s7, v0
	v_cmp_eq_u32_e32 vcc, 0, v0
	s_waitcnt vmcnt(0)
	s_and_saveexec_b64 s[10:11], vcc
	s_cbranch_execz .LBB0_827
	s_add_i32 s76, s8, 0x900
	s_lshl_b64 s[8:9], s[76:77], 2
	v_readlane_b32 s12, v254, 46
	v_readlane_b32 s13, v254, 47
	s_add_u32 s8, s12, s8
	s_addc_u32 s9, s13, s9
	s_bcnt1_i32_b64 s6, s[6:7]
	v_mov_b32_e32 v0, s6
.LBB0_827:
	s_or_b64 exec, exec, s[10:11]
	s_waitcnt vmcnt(0)

.LBB0_914:
	s_or_b64 exec, exec, s[4:5]
	s_waitcnt vmcnt(0)
	v_readfirstlane_b32 s2, v3
	v_sub_u32_e32 v4, 0, v2
	s_mov_b64 s[6:7], -1
	v_add_u32_e32 v3, s2, v0
	v_cvt_f32_u32_e32 v0, v2
	v_readlane_b32 s2, v254, 46
	v_readlane_b32 s3, v254, 47
	s_add_u32 s2, s2, 0x3500
	v_rcp_iflag_f32_e32 v0, v0
	s_addc_u32 s3, s3, 0
	v_mul_f32_e32 v0, 0x4f7ffffe, v0
	v_cvt_u32_f32_e32 v0, v0
	v_mul_lo_u32 v4, v4, v0
	v_mul_hi_u32 v4, v0, v4
	v_add_u32_e32 v0, v0, v4
	v_mul_hi_u32 v0, v3, v0
	v_mul_lo_u32 v4, v0, v2
	v_sub_u32_e32 v4, v3, v4
	v_cmp_ge_u32_e32 vcc, v4, v2
	v_add_u32_e32 v5, 1, v0
	v_add_u32_e32 v3, 1, v3
	v_cndmask_b32_e32 v0, v0, v5, vcc
	v_sub_u32_e32 v5, v4, v2
	v_cndmask_b32_e32 v4, v4, v5, vcc
	v_cmp_ge_u32_e32 vcc, v4, v2
	v_add_u32_e32 v4, 1, v0
	s_nop 0
	v_cndmask_b32_e32 v0, v0, v4, vcc
	v_mul_lo_u32 v4, v2, v0
	v_add_u32_e32 v2, v4, v2
	v_cmp_ne_u32_e32 vcc, v3, v2
	s_cbranch_vccnz .Lxr_4
	v_readlane_b32 s98, v254, 9
	v_readlane_b32 s99, v254, 10
	v_mov_b32_e32 v100, 0x2400
	v_mov_b32_e32 v101, 1
	s_nop 4
	global_atomic_add v100, v101, s[98:99]
	global_atomic_add v100, v101, s[98:99] offset:256
	global_atomic_add v100, v101, s[98:99] offset:512
	global_atomic_add v100, v101, s[98:99] offset:768
	global_atomic_add v100, v101, s[98:99] offset:1024
	global_atomic_add v100, v101, s[98:99] offset:1280
	global_atomic_add v100, v101, s[98:99] offset:1536
	global_atomic_add v100, v101, s[98:99] offset:1792
	global_atomic_add v100, v101, s[98:99] offset:2048
	global_atomic_add v100, v101, s[98:99] offset:2304
	global_atomic_add v100, v101, s[98:99] offset:2560
	global_atomic_add v100, v101, s[98:99] offset:2816
	global_atomic_add v100, v101, s[98:99] offset:3072
	global_atomic_add v100, v101, s[98:99] offset:3328
	global_atomic_add v100, v101, s[98:99] offset:3584
	global_atomic_add v100, v101, s[98:99] offset:3840
.Lxr_4:
	v_mov_b64_e32 v[2:3], s[2:3]
	s_and_saveexec_b64 s[4:5], vcc
	s_cbranch_execz .LBB0_926
	global_load_dword v2, v1, s[2:3] sc1
	s_mov_b64 s[8:9], 0
	s_waitcnt vmcnt(0)
	v_cmp_eq_u32_e32 vcc, v2, v0
	s_and_saveexec_b64 s[6:7], vcc
	s_cbranch_execz .LBB0_925
	v_readlane_b32 s8, v254, 46
	v_readlane_b32 s9, v254, 47
	s_add_u32 s8, s8, 0x200
	s_addc_u32 s9, s9, 0
	s_mov_b32 s21, 1
	s_mov_b64 s[10:11], 0
	s_branch .LBB0_918

.LBB0_928:
	s_or_b64 exec, exec, s[2:3]
	s_mov_b64 s[2:3], exec
	v_mbcnt_lo_u32_b32 v0, s2, 0
	v_mbcnt_hi_u32_b32 v0, s3, v0
	v_cmp_eq_u32_e32 vcc, 0, v0
	s_waitcnt vmcnt(0)
	s_and_saveexec_b64 s[4:5], vcc
	s_cbranch_execz .LBB0_930
	s_add_i32 s76, s20, 0x900
	s_lshl_b64 s[6:7], s[76:77], 2
	v_readlane_b32 s8, v254, 46
	v_readlane_b32 s9, v254, 47
	s_add_u32 s6, s8, s6
	s_addc_u32 s7, s9, s7
	s_bcnt1_i32_b64 s2, s[2:3]
	v_mov_b32_e32 v0, s2
.LBB0_930:
	s_or_b64 exec, exec, s[4:5]
	s_waitcnt vmcnt(0)

.LBB0_1114:
	s_or_b64 exec, exec, s[6:7]
	s_waitcnt vmcnt(0)
	v_readfirstlane_b32 s4, v3
	v_sub_u32_e32 v4, 0, v2
	s_mov_b64 s[8:9], -1
	v_add_u32_e32 v3, s4, v0
	v_cvt_f32_u32_e32 v0, v2
	v_readlane_b32 s4, v254, 46
	v_readlane_b32 s5, v254, 47
	s_add_u32 s4, s4, 0x3500
	v_rcp_iflag_f32_e32 v0, v0
	s_addc_u32 s5, s5, 0
	v_mul_f32_e32 v0, 0x4f7ffffe, v0
	v_cvt_u32_f32_e32 v0, v0
	v_mul_lo_u32 v4, v4, v0
	v_mul_hi_u32 v4, v0, v4
	v_add_u32_e32 v0, v0, v4
	v_mul_hi_u32 v0, v3, v0
	v_mul_lo_u32 v4, v0, v2
	v_sub_u32_e32 v4, v3, v4
	v_cmp_ge_u32_e32 vcc, v4, v2
	v_add_u32_e32 v5, 1, v0
	v_add_u32_e32 v3, 1, v3
	v_cndmask_b32_e32 v0, v0, v5, vcc
	v_sub_u32_e32 v5, v4, v2
	v_cndmask_b32_e32 v4, v4, v5, vcc
	v_cmp_ge_u32_e32 vcc, v4, v2
	v_add_u32_e32 v4, 1, v0
	s_nop 0
	v_cndmask_b32_e32 v0, v0, v4, vcc
	v_mul_lo_u32 v4, v2, v0
	v_add_u32_e32 v2, v4, v2
	v_cmp_ne_u32_e32 vcc, v3, v2
	s_cbranch_vccnz .Lxr_5
	v_readlane_b32 s98, v254, 9
	v_readlane_b32 s99, v254, 10
	v_mov_b32_e32 v100, 0x2400
	v_mov_b32_e32 v101, 1
	s_nop 4
	global_atomic_add v100, v101, s[98:99]
	global_atomic_add v100, v101, s[98:99] offset:256
	global_atomic_add v100, v101, s[98:99] offset:512
	global_atomic_add v100, v101, s[98:99] offset:768
	global_atomic_add v100, v101, s[98:99] offset:1024
	global_atomic_add v100, v101, s[98:99] offset:1280
	global_atomic_add v100, v101, s[98:99] offset:1536
	global_atomic_add v100, v101, s[98:99] offset:1792
	global_atomic_add v100, v101, s[98:99] offset:2048
	global_atomic_add v100, v101, s[98:99] offset:2304
	global_atomic_add v100, v101, s[98:99] offset:2560
	global_atomic_add v100, v101, s[98:99] offset:2816
	global_atomic_add v100, v101, s[98:99] offset:3072
	global_atomic_add v100, v101, s[98:99] offset:3328
	global_atomic_add v100, v101, s[98:99] offset:3584
	global_atomic_add v100, v101, s[98:99] offset:3840
.Lxr_5:
	v_mov_b64_e32 v[2:3], s[4:5]
	s_and_saveexec_b64 s[6:7], vcc
	s_cbranch_execz .LBB0_1126
	global_load_dword v2, v1, s[4:5] sc1
	s_mov_b64 s[10:11], 0
	s_waitcnt vmcnt(0)
	v_cmp_eq_u32_e32 vcc, v2, v0
	s_and_saveexec_b64 s[8:9], vcc
	s_cbranch_execz .LBB0_1125
	v_readlane_b32 s10, v254, 46
	v_readlane_b32 s11, v254, 47
	s_add_u32 s10, s10, 0x200
	s_addc_u32 s11, s11, 0
	s_mov_b32 s24, 1
	s_mov_b64 s[12:13], 0
	s_branch .LBB0_1118

.LBB0_1128:
	s_or_b64 exec, exec, s[4:5]
	s_mov_b64 s[4:5], exec
	v_mbcnt_lo_u32_b32 v0, s4, 0
	v_mbcnt_hi_u32_b32 v0, s5, v0
	v_cmp_eq_u32_e32 vcc, 0, v0
	s_waitcnt vmcnt(0)
	s_and_saveexec_b64 s[6:7], vcc
	s_cbranch_execz .LBB0_1130
	s_add_i32 s76, s23, 0x900
	s_lshl_b64 s[8:9], s[76:77], 2
	v_readlane_b32 s10, v254, 46
	v_readlane_b32 s11, v254, 47
	s_add_u32 s8, s10, s8
	s_addc_u32 s9, s11, s9
	s_bcnt1_i32_b64 s4, s[4:5]
	v_mov_b32_e32 v0, s4
.LBB0_1130:
	s_or_b64 exec, exec, s[6:7]
	s_waitcnt vmcnt(0)

.Lxr_6:
	v_mov_b64_e32 v[2:3], s[4:5]
	s_and_saveexec_b64 s[6:7], vcc
	s_cbranch_execz .LBB0_1213
	global_load_dword v2, v1, s[4:5] sc1
	s_mov_b64 s[10:11], 0
	s_waitcnt vmcnt(0)
	v_cmp_eq_u32_e32 vcc, v2, v0
	s_and_saveexec_b64 s[8:9], vcc
	s_cbranch_execz .LBB0_1212
	v_readlane_b32 s10, v254, 46
	v_readlane_b32 s11, v254, 47
	s_add_u32 s10, s10, 0x200
	s_addc_u32 s11, s11, 0
	s_mov_b32 s23, 1
	s_mov_b64 s[12:13], 0
	s_branch .LBB0_1205

.LBB0_1215:
	s_or_b64 exec, exec, s[4:5]
	s_mov_b64 s[4:5], exec
	v_mbcnt_lo_u32_b32 v0, s4, 0
	v_mbcnt_hi_u32_b32 v0, s5, v0
	v_cmp_eq_u32_e32 vcc, 0, v0
	s_waitcnt vmcnt(0)
	s_and_saveexec_b64 s[6:7], vcc
	s_cbranch_execz .LBB0_1217
	s_add_i32 s76, s22, 0x900
	s_lshl_b64 s[8:9], s[76:77], 2
	v_readlane_b32 s10, v254, 46
	v_readlane_b32 s11, v254, 47
	s_add_u32 s8, s10, s8
	s_addc_u32 s9, s11, s9
	s_bcnt1_i32_b64 s4, s[4:5]
	v_mov_b32_e32 v0, s4
.LBB0_1217:
	s_or_b64 exec, exec, s[6:7]
	s_waitcnt vmcnt(0)

.LBB0_1336:
	s_or_b64 exec, exec, s[2:3]
	s_mov_b64 s[2:3], exec
	v_mbcnt_lo_u32_b32 v0, s2, 0
	v_mbcnt_hi_u32_b32 v0, s3, v0
	v_cmp_eq_u32_e32 vcc, 0, v0
	s_waitcnt vmcnt(0)
	s_and_saveexec_b64 s[4:5], vcc
	s_cbranch_execz .LBB0_1338
	s_add_i32 s76, s20, 0x900
	s_lshl_b64 s[6:7], s[76:77], 2
	v_readlane_b32 s8, v254, 46
	v_readlane_b32 s9, v254, 47
	s_add_u32 s6, s8, s6
	s_addc_u32 s7, s9, s7
	s_bcnt1_i32_b64 s2, s[2:3]
	v_mov_b32_e32 v0, s2
.LBB0_1338:
	s_or_b64 exec, exec, s[4:5]
	s_waitcnt vmcnt(0)

.LBB0_1685:
	s_or_b64 exec, exec, s[4:5]
	s_mov_b64 s[4:5], exec
	v_mbcnt_lo_u32_b32 v0, s4, 0
	v_mbcnt_hi_u32_b32 v0, s5, v0
	v_cmp_eq_u32_e32 vcc, 0, v0
	s_waitcnt vmcnt(0)
	s_and_saveexec_b64 s[6:7], vcc
	s_cbranch_execz .LBB0_1687
	s_add_i32 s76, s23, 0x900
	s_lshl_b64 s[8:9], s[76:77], 2
	v_readlane_b32 s10, v254, 46
	v_readlane_b32 s11, v254, 47
	s_add_u32 s8, s10, s8
	s_addc_u32 s9, s11, s9
	s_bcnt1_i32_b64 s4, s[4:5]
	v_mov_b32_e32 v0, s4
.LBB0_1687:
	s_or_b64 exec, exec, s[6:7]
	s_waitcnt vmcnt(0)

.LBB0_1778:
	s_or_b64 exec, exec, s[2:3]
	s_mov_b64 s[2:3], exec
	v_mbcnt_lo_u32_b32 v0, s2, 0
	v_mbcnt_hi_u32_b32 v0, s3, v0
	v_cmp_eq_u32_e32 vcc, 0, v0
	s_waitcnt vmcnt(0)
	s_and_saveexec_b64 s[4:5], vcc
	s_cbranch_execz .LBB0_1780
	s_add_i32 s76, s20, 0x900
	s_lshl_b64 s[6:7], s[76:77], 2
	v_readlane_b32 s8, v254, 46
	v_readlane_b32 s9, v254, 47
	s_add_u32 s6, s8, s6
	s_addc_u32 s7, s9, s7
	s_bcnt1_i32_b64 s2, s[2:3]
	v_mov_b32_e32 v0, s2
.LBB0_1780:
	s_or_b64 exec, exec, s[4:5]
	s_waitcnt vmcnt(0)

.LBB0_1928:
	s_or_b64 exec, exec, s[2:3]
	s_mov_b64 s[2:3], exec
	v_mbcnt_lo_u32_b32 v0, s2, 0
	v_mbcnt_hi_u32_b32 v0, s3, v0
	v_cmp_eq_u32_e32 vcc, 0, v0
	s_waitcnt vmcnt(0)
	s_and_saveexec_b64 s[4:5], vcc
	s_cbranch_execz .LBB0_1930
	s_add_i32 s76, s20, 0x900
	s_lshl_b64 s[6:7], s[76:77], 2
	v_readlane_b32 s8, v254, 46
	v_readlane_b32 s9, v254, 47
	s_add_u32 s6, s8, s6
	s_addc_u32 s7, s9, s7
	s_bcnt1_i32_b64 s2, s[2:3]
	v_mov_b32_e32 v0, s2
.LBB0_1930:
	s_or_b64 exec, exec, s[4:5]
	s_waitcnt vmcnt(0)
